# k40: k35 + P2->P3 grid barrier with early arrival (converting workgroups arrive at the start of P2, GEMM workgroups after their last GEMM unit; everyone waits at the end of P2), under the same run-tim
# speedup vs baseline: 1.0128x; 1.0050x over previous
; __device__ __forceinline__ unsigned xb_add(unsigned* p, unsigned v) { return __hip_atomic_fetch_add(p, v, __ATOMIC_RELAXED, __HIP_MEMORY_SCOPE_AGENT); }
; __device__ __forceinline__ void xcd_barrier(const XcdBarrier& b) {
;     ...
;         const unsigned old = xb_add(&bar[XB_XSUB(b.x)], 1u);
;         const unsigned gen = old / nloc;
;         if (old + 1u == (gen + 1u) * nloc) {
;             __builtin_amdgcn_fence(__ATOMIC_RELEASE, "agent");
;             asm volatile("s_waitcnt vmcnt(0)" ::: "memory");
;             const unsigned og = xb_add(&bar[XB_TOP], 1u);
;             const unsigned tg = og / nx;
;             if (og + 1u == (tg + 1u) * nx) xb_add(&bar[XB_TOPGEN], 1u);
; __global__ void __launch_bounds__(NWAVES * 64, 2) fwd_kernel(Args args) {
;     ...
;         const bool split2 = (G == 256); const int xcd2 = bx & 7, slot2 = bx >> 3;
;         if (!split2 || slot2 < T8_GS) {
;         SchedDense S; S.init(Z_FP8 ? (const void*)XN8 : (const void*)XN, WinT, T, INW, D, D, split2 ? T8_GS * 8 : G, split2 ? slot2 * 8 + xcd2 : bx, Z_FP8 ? 1 : 2);
;         EpiZ E{UP, UG, SGP, SGS, Z_FP8 ? 0.03125f : 1.0f};
;         pg8::gemm_phase<EpiZ, SchedDense, false, Z_FP8 ? 1 : 2>(lds + RING_OFF, D, D, D, S, E);
;         } else { constexpr int TRB = 256 * 144; T8_CONSTS; T8_RUN(U_TOT - T8_NMOVE + (slot2 - T8_GS) * 8 + xcd2, (32 - T8_GS) * 8, U_TOT); }
.LBB0_431:
	s_cmp_lt_i32 s94, 3
	s_cselect_b64 s[4:5], -1, 0
	s_cmp_gt_i32 s95, 2
	s_cselect_b64 s[6:7], -1, 0
	s_and_b64 s[4:5], s[4:5], s[6:7]
	s_andn2_b64 vcc, exec, s[4:5]
	s_cbranch_vccnz .LBB0_615
	v_readlane_b32 s4, v254, 1
	v_readlane_b32 s5, v254, 2
	s_cmpk_lg_i32 s50, 0x100
	s_load_dwordx2 s[8:9], s[4:5], 0xf8
	s_cselect_b64 s[12:13], -1, 0
	s_cmpk_eq_i32 s50, 0x100
	s_cselect_b64 s[6:7], -1, 0
	s_cmpk_gt_i32 s2, 0x7f
	s_cselect_b64 s[10:11], -1, 0
	s_and_b64 s[10:11], s[10:11], s[6:7]
	s_mov_b64 s[6:7], -1
	s_and_b64 vcc, exec, s[10:11]
	s_cbranch_vccz .LBB0_464
	v_readlane_b32 s98, v254, 40
	s_cmp_lg_u32 s98, 0
	s_cbranch_scc1 .La3c_done
	s_cmpk_lg_i32 s50, 0x100
	s_cbranch_scc1 .La3c_done
	s_cmp_lt_i32 s95, 4
	s_cbranch_scc1 .La3c_done
	s_and_saveexec_b64 s[100:101], s[88:89]
	s_cbranch_execz .La3c_x
	s_lshl_b32 s98, s0, 8
	s_add_i32 s98, s98, 0x1400
	v_mov_b32_e32 v252, s98
	v_mov_b32_e32 v251, 1
	global_atomic_add v253, v252, v251, s[96:97] sc0
	s_waitcnt vmcnt(0)
	v_readfirstlane_b32 s99, v253
	s_add_i32 s99, s99, 1
	s_and_b32 s99, s99, 31
	s_cmp_eq_u32 s99, 0
	s_cbranch_scc0 .La3c_x
	buffer_wbl2 sc1
	s_waitcnt vmcnt(0)
	s_add_i32 s98, s98, 0x1000
	v_mov_b32_e32 v252, s98
	global_atomic_add v252, v251, s[96:97]
	v_mov_b32_e32 v252, 0x3400
	global_atomic_add v253, v252, v251, s[96:97] sc0
	s_waitcnt vmcnt(0)
	v_readfirstlane_b32 s99, v253
	s_add_i32 s99, s99, 1
	s_and_b32 s99, s99, 7
	s_cmp_eq_u32 s99, 0
	s_cbranch_scc0 .La3c_x
	v_mov_b32_e32 v252, 0x3500
	global_atomic_add v252, v251, s[96:97]

; __global__ void __launch_bounds__(NWAVES * 64, 2) fwd_kernel(Args args) {
;     ...
;                 T8_RUN(vcu, G, (G == 256) ? U_TOT - T8_NMOVE : U_TOT);
;     ...
;         } else { constexpr int TRB = 256 * 144; T8_CONSTS; T8_RUN(U_TOT - T8_NMOVE + (slot2 - T8_GS) * 8 + xcd2, (32 - T8_GS) * 8, U_TOT); }
.La3c_done:
	s_movk_i32 s98, 0x2fc0
	s_movk_i32 s99, 0x2f40
	s_movk_i32 s100, 0x2ec0
	s_movk_i32 s101, 0x740

; #define PG8_WAIT_V(n) asm volatile("s_waitcnt vmcnt(" #n ")" ::: "memory")
; #define PG8_BAR __builtin_amdgcn_s_barrier()
; __device__ __forceinline__ unsigned xb_add(unsigned* p, unsigned v) { return __hip_atomic_fetch_add(p, v, __ATOMIC_RELAXED, __HIP_MEMORY_SCOPE_AGENT); }
;     ...
;     PG8_WAIT_V(0);
;     PG8_BAR;
; __device__ __forceinline__ void xcd_barrier(const XcdBarrier& b) {
;     ...
;         const unsigned old = xb_add(&bar[XB_XSUB(b.x)], 1u);
;         const unsigned gen = old / nloc;
;         if (old + 1u == (gen + 1u) * nloc) {
;             __builtin_amdgcn_fence(__ATOMIC_RELEASE, "agent");
;             asm volatile("s_waitcnt vmcnt(0)" ::: "memory");
;             const unsigned og = xb_add(&bar[XB_TOP], 1u);
;             const unsigned tg = og / nx;
;             if (og + 1u == (tg + 1u) * nx) xb_add(&bar[XB_TOPGEN], 1u);
.LBB0_560:
	s_waitcnt vmcnt(0)
	s_barrier
	v_readlane_b32 s98, v254, 40
	s_cmp_lg_u32 s98, 0
	s_cbranch_scc1 .La3g_done
	s_cmpk_lg_i32 s50, 0x100
	s_cbranch_scc1 .La3g_done
	s_cmp_lt_i32 s95, 4
	s_cbranch_scc1 .La3g_done
	s_and_saveexec_b64 s[100:101], s[88:89]
	s_cbranch_execz .La3g_x
	s_lshl_b32 s98, s0, 8
	s_add_i32 s98, s98, 0x1400
	v_mov_b32_e32 v252, s98
	v_mov_b32_e32 v251, 1
	global_atomic_add v253, v252, v251, s[96:97] sc0
	s_waitcnt vmcnt(0)
	v_readfirstlane_b32 s99, v253
	s_add_i32 s99, s99, 1
	s_and_b32 s99, s99, 31
	s_cmp_eq_u32 s99, 0
	s_cbranch_scc0 .La3g_x
	buffer_wbl2 sc1
	s_waitcnt vmcnt(0)
	s_add_i32 s98, s98, 0x1000
	v_mov_b32_e32 v252, s98
	global_atomic_add v252, v251, s[96:97]
	v_mov_b32_e32 v252, 0x3400
	global_atomic_add v253, v252, v251, s[96:97] sc0
	s_waitcnt vmcnt(0)
	v_readfirstlane_b32 s99, v253
	s_add_i32 s99, s99, 1
	s_and_b32 s99, s99, 7
	s_cmp_eq_u32 s99, 0
	s_cbranch_scc0 .La3g_x
	v_mov_b32_e32 v252, 0x3500
	global_atomic_add v252, v251, s[96:97]

; #define PG8_WAIT_V(n) asm volatile("s_waitcnt vmcnt(" #n ")" ::: "memory")
; #define PG8_BAR __builtin_amdgcn_s_barrier()
; __device__ __forceinline__ unsigned xb_ld(unsigned* p)              { return __hip_atomic_load(p, __ATOMIC_RELAXED, __HIP_MEMORY_SCOPE_AGENT); }
; __device__ __forceinline__ unsigned xb_add(unsigned* p, unsigned v) { return __hip_atomic_fetch_add(p, v, __ATOMIC_RELAXED, __HIP_MEMORY_SCOPE_AGENT); }
; #define XB_SPIN(cond, bar) do { unsigned _sp = 0; while (cond) { __builtin_amdgcn_s_sleep(1); \
;     if ((++_sp & 255u) == 0u) { if (xb_ld(&(bar)[XB_TMO])) break; if (_sp > XB_SPIN_CAP) { atomicAdd(&(bar)[XB_TMO], 1u); break; } } } } while (0)
;     ...
;     PG8_WAIT_V(0);
;     PG8_BAR;
; __device__ __forceinline__ void xcd_barrier(const XcdBarrier& b) {
;     ...
;             else XB_SPIN(xb_ld(&bar[XB_TOPGEN]) == tg, bar);
;             __builtin_amdgcn_fence(__ATOMIC_ACQUIRE, "agent");
;             xb_add(&bar[XB_XGEN(b.x)], 1u);
;             asm volatile("s_waitcnt vmcnt(0)" ::: "memory");
;         } else {
;             XB_SPIN(xb_ld(&bar[XB_XGEN(b.x)]) == gen, bar);
; __global__ void __launch_bounds__(NWAVES * 64, 2) fwd_kernel(Args args) {
;     ...
;                 T8_RUN(vcu, G, (G == 256) ? U_TOT - T8_NMOVE : U_TOT);
.La3g_done:
	v_readlane_b32 s4, v254, 1
	v_readlane_b32 s5, v254, 2
	s_movk_i32 s98, 0x32c0
	s_movk_i32 s99, 0x3240
	s_movk_i32 s100, 0x31c0
	s_movk_i32 s101, 0x2fc0
	s_load_dwordx2 s[8:9], s[4:5], 0xf8
	s_branch .Lp2_conv_entry
.LBB0_561:
	s_cmp_lt_i32 s95, 4
	s_cbranch_scc1 .LBB0_615
	v_readlane_b32 s98, v254, 40
	s_cmp_lg_u32 s98, 0
	s_cbranch_scc1 .Lb3_full
	s_cmpk_lg_i32 s50, 0x100
	s_cbranch_scc1 .Lb3_full
	s_and_saveexec_b64 s[100:101], s[88:89]
	s_cbranch_execz .Lb3_wait_done
	s_mov_b32 s98, 0
	v_mov_b32_e32 v252, 0x3500
.Lb3_poll:
	global_load_dword v253, v252, s[96:97] sc1
	s_waitcnt vmcnt(0)
	v_readfirstlane_b32 s99, v253
	s_cmp_ge_u32 s99, 3
	s_cbranch_scc1 .Lb3_seen
	s_sleep 1
	s_add_i32 s98, s98, 1
	s_cmp_lt_u32 s98, 0x100000
	s_cbranch_scc1 .Lb3_poll

; __device__ __forceinline__ unsigned xb_ld(unsigned* p)              { return __hip_atomic_load(p, __ATOMIC_RELAXED, __HIP_MEMORY_SCOPE_AGENT); }
; __device__ __forceinline__ unsigned xb_add(unsigned* p, unsigned v) { return __hip_atomic_fetch_add(p, v, __ATOMIC_RELAXED, __HIP_MEMORY_SCOPE_AGENT); }
; #define XB_SPIN(cond, bar) do { unsigned _sp = 0; while (cond) { __builtin_amdgcn_s_sleep(1); \
;     if ((++_sp & 255u) == 0u) { if (xb_ld(&(bar)[XB_TMO])) break; if (_sp > XB_SPIN_CAP) { atomicAdd(&(bar)[XB_TMO], 1u); break; } } } } while (0)
; #define GRID_BAR() do { if (N_LAUNCHES == 1) xcd_barrier(bar); } while (0)
; #define BOTH(k) (IN(k) && IN((k) + 1))
; #define PROBE_MID(k) do { if (PROBE_PH == (k) && PROBE_MODE == 0) { __syncthreads(); pr_dt = __builtin_amdgcn_s_memrealtime() - pr_t0; } } while (0)
; #define PROBE_END(k) do { if (PROBE_PH == (k) && PROBE_MODE == 1) { pr_dt = __builtin_amdgcn_s_memrealtime() - pr_t0; } } while (0)
; __device__ __forceinline__ void xcd_barrier(const XcdBarrier& b) {
;     ...
;             else XB_SPIN(xb_ld(&bar[XB_TOPGEN]) == tg, bar);
;             __builtin_amdgcn_fence(__ATOMIC_ACQUIRE, "agent");
;             xb_add(&bar[XB_XGEN(b.x)], 1u);
;             asm volatile("s_waitcnt vmcnt(0)" ::: "memory");
;         } else {
;             XB_SPIN(xb_ld(&bar[XB_XGEN(b.x)]) == gen, bar);
;             __builtin_amdgcn_fence(__ATOMIC_ACQUIRE, "agent");
;             asm volatile("s_waitcnt vmcnt(0)" ::: "memory");
;         }
;     }
;     __syncthreads();
; __global__ void __launch_bounds__(NWAVES * 64, 2) fwd_kernel(Args args) {
;     ...
;         PROBE_MID(2); if (BOTH(2)) GRID_BAR(); PROBE_END(2);
.Lb3_wait_done:
	s_or_b64 exec, exec, s[100:101]
	s_waitcnt lgkmcnt(0)
	s_barrier
	s_branch .LBB0_615
.Lb3_full:
	s_waitcnt vmcnt(0)
	s_waitcnt vmcnt(0) lgkmcnt(0)
	s_barrier
	s_and_saveexec_b64 s[4:5], s[88:89]
	s_cbranch_execz .LBB0_614
	s_add_i32 s3, 0, 0x20160
	v_mov_b32_e32 v1, s3
	s_waitcnt vmcnt(0) expcnt(0) lgkmcnt(0)
	ds_read_b32 v3, v1
	s_add_i32 s3, 0, 0x20164
	v_mov_b32_e32 v1, s3
	ds_read_b32 v1, v1
	s_waitcnt lgkmcnt(1)
	v_cmp_ne_u32_e32 vcc, 0, v3
	s_cbranch_vccnz .LBB0_578
	v_readlane_b32 s6, v254, 3
	v_readlane_b32 s7, v254, 4
	s_load_dwordx2 s[10:11], s[6:7], 0x4
	v_readlane_b32 s34, v254, 5
	v_readlane_b32 s35, v254, 6
	s_add_u32 s6, s34, 0x4200
	s_addc_u32 s7, s35, 0
	s_add_u32 s8, s34, 0x4400
	s_addc_u32 s9, s35, 0
	s_waitcnt lgkmcnt(0)
	s_mul_i32 s3, s10, s50
	s_add_u32 s10, s34, 0x4500
	s_mul_i32 s3, s3, s11
	s_addc_u32 s11, s35, 0
	s_add_u32 s12, s34, 0x4600
	s_addc_u32 s13, s35, 0
	s_add_u32 s14, s34, 0x4700
	s_addc_u32 s15, s35, 0
	s_add_u32 s16, s34, 0x4800
	s_addc_u32 s17, s35, 0
	s_add_u32 s18, s34, 0x4900
	s_addc_u32 s19, s35, 0
	s_add_u32 s20, s34, 0x4a00
	s_addc_u32 s21, s35, 0
	s_add_u32 s22, s34, 0x4b00
	s_addc_u32 s23, s35, 0
	s_add_u32 s24, s34, 0x4c00
	s_addc_u32 s25, s35, 0
	s_add_u32 s26, s34, 0x4d00
	s_addc_u32 s27, s35, 0
	s_add_u32 s28, s34, 0x4e00
	s_addc_u32 s29, s35, 0
	s_add_u32 s30, s34, 0x4f00
	s_addc_u32 s31, s35, 0
	s_add_u32 s36, s34, 0x5000
	s_addc_u32 s37, s35, 0
	s_add_u32 s38, s34, 0x5100
	s_addc_u32 s39, s35, 0
	s_add_u32 s40, s34, 0x5200
	s_addc_u32 s41, s35, 0
	s_add_u32 s42, s34, 0x5300
	s_addc_u32 s43, s35, 0
	s_mov_b32 s33, 1
	v_mov_b32_e32 v17, 0
	s_branch .LBB0_566
